# gemm1 trailing blocks: hipcc's 18-round-trip edge bucketing replaced by hand-written version (all edge loads in one trip, one atomic, one scatter); plus sc1 on gemm1 weight loads and agg stores, agg b
# speedup vs baseline: 1.0265x; 1.0265x over previous
_Z11gemm_kernelILb1EEvPKviiiPKDF16_PDF16_PfS5_PKfS7_ii8PrepArgs:
	s_load_dwordx2 s[16:17], s[0:1], 0x48
	s_load_dwordx4 s[20:23], s[0:1], 0x110
	s_load_dwordx4 s[24:27], s[0:1], 0x128
	s_load_dwordx2 s[28:29], s[0:1], 0x138
	s_mov_b64 s[4:5], -1
	s_waitcnt lgkmcnt(0)
	s_mov_b32 s18, s17
	s_cmp_lt_i32 s2, s17
	s_cbranch_scc1 .LBB6_97
	s_sub_i32 s2, s2, s17
.Lmy_bucket:
	s_mov_b64 s[50:51], exec
	v_lshlrev_b32_e32 v1, 2, v0
	v_mov_b32_e32 v2, 0
	s_movk_i32 s33, 0x100
	v_cmp_gt_u32_e32 vcc, s33, v0
	s_and_saveexec_b64 s[30:31], vcc
	ds_write_b32 v1, v2
	s_mov_b64 exec, s[50:51]
	s_mul_i32 s32, s2, 0x8b3
	v_add_u32_e32 v3, s32, v0
	v_lshlrev_b32_e32 v4, 2, v3
	s_movk_i32 s33, 0x8b3
	s_mov_b32 s34, 0x8b290
	v_cmp_gt_u32_e32 vcc, s33, v0
	v_cmp_gt_u32_e64 s[46:47], s34, v3
	s_and_b64 s[36:37], vcc, s[46:47]
	v_add_u32_e32 v5, 512, v0
	v_add_u32_e32 v6, 512, v3
	v_cmp_gt_u32_e32 vcc, s33, v5
	v_cmp_gt_u32_e64 s[46:47], s34, v6
	s_and_b64 s[38:39], vcc, s[46:47]
	v_add_u32_e32 v5, 1024, v0
	v_add_u32_e32 v6, 1024, v3
	v_cmp_gt_u32_e32 vcc, s33, v5
	v_cmp_gt_u32_e64 s[46:47], s34, v6
	s_and_b64 s[40:41], vcc, s[46:47]
	v_add_u32_e32 v5, 1536, v0
	v_add_u32_e32 v6, 1536, v3
	v_cmp_gt_u32_e32 vcc, s33, v5
	v_cmp_gt_u32_e64 s[46:47], s34, v6
	s_and_b64 s[42:43], vcc, s[46:47]
	v_add_u32_e32 v5, 2048, v0
	v_add_u32_e32 v6, 2048, v3
	v_cmp_gt_u32_e32 vcc, s33, v5
	v_cmp_gt_u32_e64 s[46:47], s34, v6
	s_and_b64 s[44:45], vcc, s[46:47]
	s_waitcnt lgkmcnt(0)
	s_mov_b64 exec, s[36:37]
	global_load_dword v10, v4, s[22:23]
	global_load_dword v11, v4, s[20:21]
	s_mov_b64 exec, s[38:39]
	v_add_u32_e32 v6, 2048, v4
	global_load_dword v12, v6, s[22:23]
	global_load_dword v13, v6, s[20:21]
	s_mov_b64 exec, s[40:41]
	v_add_u32_e32 v7, 4096, v4
	global_load_dword v14, v7, s[22:23]
	global_load_dword v15, v7, s[20:21]
	s_mov_b64 exec, s[42:43]
	v_add_u32_e32 v8, 6144, v4
	global_load_dword v16, v8, s[22:23]
	global_load_dword v17, v8, s[20:21]
	s_mov_b64 exec, s[44:45]
	v_add_u32_e32 v9, 8192, v4
	global_load_dword v18, v9, s[22:23]
	global_load_dword v19, v9, s[20:21]
	s_mov_b64 exec, s[50:51]
	v_mov_b32_e32 v35, 1
	v_mov_b32_e32 v36, 0x8ada
	s_waitcnt lgkmcnt(0)
	s_barrier
	s_waitcnt vmcnt(0)
	s_mov_b64 exec, s[36:37]
	v_mul_u32_u24_e32 v20, v10, v36
	v_lshrrev_b32_e32 v20, 22, v20
	v_lshlrev_b32_e32 v37, 2, v20
	ds_add_rtn_u32 v25, v37, v35
	s_mov_b64 exec, s[38:39]
	v_mul_u32_u24_e32 v21, v12, v36
	v_lshrrev_b32_e32 v21, 22, v21
	v_lshlrev_b32_e32 v37, 2, v21
	ds_add_rtn_u32 v26, v37, v35
	s_mov_b64 exec, s[40:41]
	v_mul_u32_u24_e32 v22, v14, v36
	v_lshrrev_b32_e32 v22, 22, v22
	v_lshlrev_b32_e32 v37, 2, v22
	ds_add_rtn_u32 v27, v37, v35
	s_mov_b64 exec, s[42:43]
	v_mul_u32_u24_e32 v23, v16, v36
	v_lshrrev_b32_e32 v23, 22, v23
	v_lshlrev_b32_e32 v37, 2, v23
	ds_add_rtn_u32 v28, v37, v35
	s_mov_b64 exec, s[44:45]
	v_mul_u32_u24_e32 v24, v18, v36
	v_lshrrev_b32_e32 v24, 22, v24
	v_lshlrev_b32_e32 v37, 2, v24
	ds_add_rtn_u32 v29, v37, v35
	s_mov_b64 exec, s[50:51]
	s_waitcnt lgkmcnt(0)
	s_barrier
	s_movk_i32 s33, 0x100
	v_cmp_gt_u32_e32 vcc, s33, v0
	s_and_saveexec_b64 s[30:31], vcc
	s_cbranch_execz .Lmy_bk_noatom
	ds_read_b32 v38, v1
	s_waitcnt lgkmcnt(0)
	v_cmp_lt_u32_e32 vcc, 0, v38
	s_and_b64 exec, exec, vcc
	s_cbranch_execz .Lmy_bk_noatom
	global_atomic_add v39, v1, v38, s[24:25] sc0
	s_waitcnt vmcnt(0)
	ds_write_b32 v1, v39 offset:1024
.Lmy_bk_noatom:
	s_mov_b64 exec, s[50:51]
	s_waitcnt lgkmcnt(0)
	s_barrier
	s_mov_b64 exec, s[36:37]
	v_lshlrev_b32_e32 v37, 2, v20
	ds_read_b32 v30, v37 offset:1024
	s_mov_b64 exec, s[38:39]
	v_lshlrev_b32_e32 v37, 2, v21
	ds_read_b32 v31, v37 offset:1024
	s_mov_b64 exec, s[40:41]
	v_lshlrev_b32_e32 v37, 2, v22
	ds_read_b32 v32, v37 offset:1024
	s_mov_b64 exec, s[42:43]
	v_lshlrev_b32_e32 v37, 2, v23
	ds_read_b32 v33, v37 offset:1024
	s_mov_b64 exec, s[44:45]
	v_lshlrev_b32_e32 v37, 2, v24
	ds_read_b32 v34, v37 offset:1024
	s_movk_i32 s33, 0x1000
	s_waitcnt lgkmcnt(0)
	s_mov_b64 exec, s[36:37]
	v_add_u32_e32 v40, v30, v25
	v_cmp_gt_u32_e32 vcc, s33, v40
	s_and_saveexec_b64 s[46:47], vcc
	v_lshl_add_u32 v41, v20, 12, v40
	v_lshlrev_b32_e32 v41, 3, v41
	global_store_dwordx2 v41, v[10:11], s[26:27]
	s_andn2_b64 exec, s[46:47], exec
	s_cbranch_execz .Lmy_bk_q0
	v_mov_b32_e32 v42, 1
	v_mov_b32_e32 v43, 0
	global_atomic_add v42, v43, v42, s[24:25] offset:1024 sc0
	s_waitcnt vmcnt(0)
	v_lshlrev_b32_e32 v42, 3, v42
	global_store_dwordx2 v42, v[10:11], s[28:29]
.Lmy_bk_q0:
	s_mov_b64 exec, s[38:39]
	v_add_u32_e32 v40, v31, v26
	v_cmp_gt_u32_e32 vcc, s33, v40
	s_and_saveexec_b64 s[46:47], vcc
	v_lshl_add_u32 v41, v21, 12, v40
	v_lshlrev_b32_e32 v41, 3, v41
	global_store_dwordx2 v41, v[12:13], s[26:27]
	s_andn2_b64 exec, s[46:47], exec
	s_cbranch_execz .Lmy_bk_q1
	v_mov_b32_e32 v42, 1
	v_mov_b32_e32 v43, 0
	global_atomic_add v42, v43, v42, s[24:25] offset:1024 sc0
	s_waitcnt vmcnt(0)
	v_lshlrev_b32_e32 v42, 3, v42
	global_store_dwordx2 v42, v[12:13], s[28:29]
.Lmy_bk_q1:
	s_mov_b64 exec, s[40:41]
	v_add_u32_e32 v40, v32, v27
	v_cmp_gt_u32_e32 vcc, s33, v40
	s_and_saveexec_b64 s[46:47], vcc
	v_lshl_add_u32 v41, v22, 12, v40
	v_lshlrev_b32_e32 v41, 3, v41
	global_store_dwordx2 v41, v[14:15], s[26:27]
	s_andn2_b64 exec, s[46:47], exec
	s_cbranch_execz .Lmy_bk_q2
	v_mov_b32_e32 v42, 1
	v_mov_b32_e32 v43, 0
	global_atomic_add v42, v43, v42, s[24:25] offset:1024 sc0
	s_waitcnt vmcnt(0)
	v_lshlrev_b32_e32 v42, 3, v42
	global_store_dwordx2 v42, v[14:15], s[28:29]
.Lmy_bk_q2:
	s_mov_b64 exec, s[42:43]
	v_add_u32_e32 v40, v33, v28
	v_cmp_gt_u32_e32 vcc, s33, v40
	s_and_saveexec_b64 s[46:47], vcc
	v_lshl_add_u32 v41, v23, 12, v40
	v_lshlrev_b32_e32 v41, 3, v41
	global_store_dwordx2 v41, v[16:17], s[26:27]
	s_andn2_b64 exec, s[46:47], exec
	s_cbranch_execz .Lmy_bk_q3
	v_mov_b32_e32 v42, 1
	v_mov_b32_e32 v43, 0
	global_atomic_add v42, v43, v42, s[24:25] offset:1024 sc0
	s_waitcnt vmcnt(0)
	v_lshlrev_b32_e32 v42, 3, v42
	global_store_dwordx2 v42, v[16:17], s[28:29]
.Lmy_bk_q3:
	s_mov_b64 exec, s[44:45]
	v_add_u32_e32 v40, v34, v29
	v_cmp_gt_u32_e32 vcc, s33, v40
	s_and_saveexec_b64 s[46:47], vcc
	v_lshl_add_u32 v41, v24, 12, v40
	v_lshlrev_b32_e32 v41, 3, v41
	global_store_dwordx2 v41, v[18:19], s[26:27]
	s_andn2_b64 exec, s[46:47], exec
	s_cbranch_execz .Lmy_bk_q4
	v_mov_b32_e32 v42, 1
	v_mov_b32_e32 v43, 0
	global_atomic_add v42, v43, v42, s[24:25] offset:1024 sc0
	s_waitcnt vmcnt(0)
	v_lshlrev_b32_e32 v42, 3, v42
	global_store_dwordx2 v42, v[18:19], s[28:29]
.Lmy_bk_q4:
	s_mov_b64 exec, s[50:51]
	s_barrier
	s_mov_b64 s[4:5], 0
